# spatial-gating unit: LayerNorm input rows requested two at a time (two memory round trips instead of four)
# baseline (speedup 1.0000x reference)
; __device__ __forceinline__ int crow(int r, int hi) { return (r & 3) + 8 * (r >> 2) + 4 * hi; }
; __device__ __forceinline__ void unit(const bf16_t* proj, const float* stats  , const float* lng, const float* lnb, const float* sw, const float* sb, bf16_t* Y2, int un, LAS unsigned char* lds) {
;     ...
;     const int g = un & 7, R0 = (un >> 3) * 128;
;     const int tb = wid & 3, eh = wid >> 2, t = tb * 32 + r32;
;     f32x4 wv[16]; unsigned uu[32], zq[32]; float bias[16];
; #pragma unroll
;     for (int i = 0; i < 8; ++i) { const int s0 = (i >> 2) * 64 + 16 * (i & 3) + hi * 8; const float* wp = sw + ((size_t)g * 128 + t) * 128 + s0; wv[2 * i] = *(const f32x4*)wp; wv[2 * i + 1] = *(const f32x4*)(wp + 4); }
; #pragma unroll
;     for (int r = 0; r < 16; ++r) { const int tr = tb * 32 + att::crow(r, hi), bt = R0 + tr; bias[r] = sb[g * 128 + tr];
; #pragma unroll
;         for (int d = 0; d < 2; ++d) { const int ch = g * 128 + (2 * eh + d) * 32 + (r32 & ~1); uu[r * 2 + d] = *(const unsigned*)(proj + (size_t)bt * NC + C_UC + ch); zq[r * 2 + d] = *(const unsigned*)(proj + (size_t)bt * NC + C_ZC + ch); } }
.LBB0_1376:
	s_andn2_b64 vcc, exec, s[0:1]
	s_cbranch_vccnz .LBB0_425
	v_readlane_b32 s4, v252, 35
	v_readlane_b32 s10, v252, 41
	v_readlane_b32 s11, v252, 42
	s_mov_b64 s[0:1], s[10:11]
	v_readlane_b32 s5, v252, 36
	v_readlane_b32 s12, v252, 43
	v_readlane_b32 s13, v252, 44
	v_readlane_b32 s10, v254, 43
	v_readlane_b32 s11, v254, 44
	s_add_u32 s0, s0, s10
	s_mov_b64 s[4:5], s[12:13]
	s_addc_u32 s1, s1, s11
	v_readlane_b32 s6, v252, 37
	v_readlane_b32 s7, v252, 38
	v_readlane_b32 s8, v252, 39
	v_readlane_b32 s9, v252, 40
	v_readlane_b32 s14, v252, 45
	v_readlane_b32 s15, v252, 46
	s_add_u32 s4, s4, s10
	s_addc_u32 s5, s5, s11
	s_mov_b64 s[6:7], s[14:15]
	v_readlane_b32 s8, v253, 54
	v_readlane_b32 s16, v252, 47
	v_readlane_b32 s17, v252, 48
	v_readlane_b32 s9, v253, 55
	s_add_u32 s12, s6, s8
	s_addc_u32 s13, s7, s9
	s_mov_b64 s[6:7], s[16:17]
	s_add_u32 s6, s6, s10
	v_readlane_b32 s8, v254, 47
	s_addc_u32 s7, s7, s11
	s_waitcnt vmcnt(23)
	v_mov_b32_e32 v176, v0
	s_and_b32 s2, s8, 7
	s_lshl_b32 s8, s8, 4
	s_add_i32 s8, s8, 0x7fffe000
	v_readfirstlane_b32 s10, v176
	s_and_b32 s11, s8, 0x7fffff80
	s_lshr_b32 s8, s10, 1
	v_and_b32_e32 v177, 31, v176
	s_and_b32 s9, s8, 0x60
	v_or_b32_e32 v182, s9, v177
	s_lshl_b32 s8, s2, 16
	s_waitcnt vmcnt(3)
	v_lshl_or_b32 v2, v182, 9, s8
	v_lshl_add_u64 v[4:5], s[12:13], 0, v[2:3]
	v_and_b32_e32 v2, 32, v176
	s_lshl_b32 s2, s2, 7
	s_ashr_i32 s8, s10, 2
	v_lshl_add_u64 v[40:41], v[4:5], 0, v[2:3]
	s_andn2_b32 s8, s8, 63
	v_and_or_b32 v2, v176, 30, s2
	s_waitcnt vmcnt(0)
	v_bfe_u32 v1, v176, 5, 1
	v_add_u32_e32 v68, s8, v2
	v_readlane_b32 s12, v253, 48
	v_lshlrev_b32_e32 v183, 3, v1
	v_lshl_or_b32 v1, v1, 2, s9
	v_ashrrev_i32_e32 v69, 31, v68
	v_readlane_b32 s13, v253, 49
	v_or_b32_e32 v2, s11, v1
	s_mov_b32 s14, 0xe800
	v_mov_b64_e32 v[100:101], s[12:13]
	v_lshlrev_b64 v[84:85], 1, v[68:69]
	v_or_b32_e32 v68, 32, v68
	v_readlane_b32 s18, v252, 49
	v_readlane_b32 s19, v252, 50
	v_mad_u64_u32 v[70:71], s[12:13], v2, s14, v[100:101]
	s_mov_b64 s[16:17], 0x4000
	v_ashrrev_i32_e32 v69, 31, v68
	v_lshl_add_u64 v[72:73], v[70:71], 0, s[16:17]
	s_mov_b64 s[18:19], 0x5000
	v_lshlrev_b64 v[86:87], 1, v[68:69]
	v_lshl_add_u64 v[70:71], v[70:71], 0, s[18:19]
	v_lshl_add_u64 v[74:75], v[72:73], 0, v[84:85]
	v_lshl_add_u64 v[68:69], v[72:73], 0, v[86:87]
	global_load_dwordx4 v[28:31], v[40:41], off offset:16
	global_load_dwordx4 v[32:35], v[40:41], off
	global_load_dwordx4 v[20:23], v[40:41], off offset:80
	global_load_dwordx4 v[24:27], v[40:41], off offset:64
	global_load_dwordx4 v[12:15], v[40:41], off offset:144
	global_load_dwordx4 v[16:19], v[40:41], off offset:128
	s_waitcnt lgkmcnt(0)
	global_load_dwordx4 v[4:7], v[40:41], off offset:208
	global_load_dwordx4 v[8:11], v[40:41], off offset:192
	global_load_dwordx4 v[60:63], v[40:41], off offset:272
	global_load_dwordx4 v[64:67], v[40:41], off offset:256
	global_load_dwordx4 v[52:55], v[40:41], off offset:336
	global_load_dwordx4 v[56:59], v[40:41], off offset:320
	global_load_dwordx4 v[44:47], v[40:41], off offset:400
	global_load_dwordx4 v[48:51], v[40:41], off offset:384
	global_load_dwordx4 v[36:39], v[40:41], off offset:464
	s_nop 0
	global_load_dwordx4 v[40:43], v[40:41], off offset:448
	v_or_b32_e32 v1, s2, v1
	global_load_dword v180, v[74:75], off
	global_load_dword v178, v[68:69], off
	v_lshl_add_u64 v[74:75], v[70:71], 0, v[84:85]
	v_lshl_add_u64 v[68:69], v[70:71], 0, v[86:87]
	global_load_dword v181, v[74:75], off
	global_load_dword v179, v[68:69], off
	v_or_b32_e32 v68, 1, v2
	v_mad_u64_u32 v[68:69], s[12:13], v68, s14, v[100:101]
	v_lshl_add_u64 v[70:71], v[68:69], 0, s[16:17]
	v_lshl_add_u64 v[68:69], v[68:69], 0, s[18:19]
	v_lshl_add_u64 v[72:73], v[70:71], 0, v[84:85]
	v_lshl_add_u64 v[70:71], v[70:71], 0, v[86:87]
	global_load_dword v173, v[72:73], off
	global_load_dword v172, v[70:71], off
	v_lshl_add_u64 v[72:73], v[68:69], 0, v[84:85]
	v_lshl_add_u64 v[68:69], v[68:69], 0, v[86:87]
	global_load_dword v174, v[68:69], off
	v_or_b32_e32 v68, 2, v2
	v_mad_u64_u32 v[68:69], s[12:13], v68, s14, v[100:101]
	v_lshl_add_u64 v[70:71], v[68:69], 0, s[16:17]
	global_load_dword v175, v[72:73], off
	v_lshl_add_u64 v[68:69], v[68:69], 0, s[18:19]
	v_lshl_add_u64 v[72:73], v[70:71], 0, v[84:85]
	v_lshl_add_u64 v[70:71], v[70:71], 0, v[86:87]
	global_load_dword v170, v[72:73], off
	global_load_dword v168, v[70:71], off
	v_lshl_add_u64 v[72:73], v[68:69], 0, v[84:85]
	v_lshl_add_u64 v[68:69], v[68:69], 0, v[86:87]
	global_load_dword v169, v[68:69], off
	v_or_b32_e32 v68, 3, v2
	v_mad_u64_u32 v[68:69], s[12:13], v68, s14, v[100:101]
	v_lshl_add_u64 v[70:71], v[68:69], 0, s[16:17]
	global_load_dword v171, v[72:73], off
	v_lshl_add_u64 v[68:69], v[68:69], 0, s[18:19]
	v_lshl_add_u64 v[72:73], v[70:71], 0, v[84:85]
	v_lshl_add_u64 v[70:71], v[70:71], 0, v[86:87]
	global_load_dword v165, v[72:73], off
	global_load_dword v164, v[70:71], off
	v_lshl_add_u64 v[72:73], v[68:69], 0, v[84:85]
	v_lshl_add_u64 v[68:69], v[68:69], 0, v[86:87]
	global_load_dword v166, v[68:69], off
	v_or_b32_e32 v68, 8, v2
	v_mad_u64_u32 v[68:69], s[12:13], v68, s14, v[100:101]
	v_lshl_add_u64 v[70:71], v[68:69], 0, s[16:17]
	global_load_dword v167, v[72:73], off
	v_lshl_add_u64 v[68:69], v[68:69], 0, s[18:19]
	v_lshl_add_u64 v[72:73], v[70:71], 0, v[84:85]
	v_lshl_add_u64 v[70:71], v[70:71], 0, v[86:87]
	global_load_dword v162, v[72:73], off
	global_load_dword v160, v[70:71], off
	v_lshl_add_u64 v[72:73], v[68:69], 0, v[84:85]
	v_lshl_add_u64 v[68:69], v[68:69], 0, v[86:87]
	global_load_dword v161, v[68:69], off
	v_or_b32_e32 v68, 9, v2
	v_mad_u64_u32 v[68:69], s[12:13], v68, s14, v[100:101]
; __device__ __forceinline__ int crow(int r, int hi) { return (r & 3) + 8 * (r >> 2) + 4 * hi; }
; __device__ __forceinline__ void unit(const bf16_t* proj, const float* stats  , const float* lng, const float* lnb, const float* sw, const float* sb, bf16_t* Y2, int un, LAS unsigned char* lds) {
;     ...
;     for (int r = 0; r < 16; ++r) { const int tr = tb * 32 + att::crow(r, hi), bt = R0 + tr; bias[r] = sb[g * 128 + tr];
; #pragma unroll
;         for (int d = 0; d < 2; ++d) { const int ch = g * 128 + (2 * eh + d) * 32 + (r32 & ~1); uu[r * 2 + d] = *(const unsigned*)(proj + (size_t)bt * NC + C_UC + ch); zq[r * 2 + d] = *(const unsigned*)(proj + (size_t)bt * NC + C_ZC + ch); } }
	v_lshl_add_u64 v[70:71], v[68:69], 0, s[16:17]
	global_load_dword v163, v[72:73], off
	v_lshl_add_u64 v[68:69], v[68:69], 0, s[18:19]
	v_lshl_add_u64 v[72:73], v[70:71], 0, v[84:85]
	v_lshl_add_u64 v[70:71], v[70:71], 0, v[86:87]
	global_load_dword v157, v[72:73], off
	global_load_dword v156, v[70:71], off
	v_lshl_add_u64 v[72:73], v[68:69], 0, v[84:85]
	v_lshl_add_u64 v[68:69], v[68:69], 0, v[86:87]
	global_load_dword v158, v[68:69], off
	v_or_b32_e32 v68, 10, v2
	v_mad_u64_u32 v[68:69], s[12:13], v68, s14, v[100:101]
	v_lshl_add_u64 v[70:71], v[68:69], 0, s[16:17]
	global_load_dword v159, v[72:73], off
	v_lshl_add_u64 v[68:69], v[68:69], 0, s[18:19]
	v_lshl_add_u64 v[72:73], v[70:71], 0, v[84:85]
	v_lshl_add_u64 v[70:71], v[70:71], 0, v[86:87]
	global_load_dword v154, v[72:73], off
	global_load_dword v152, v[70:71], off
	v_lshl_add_u64 v[72:73], v[68:69], 0, v[84:85]
	v_lshl_add_u64 v[68:69], v[68:69], 0, v[86:87]
	global_load_dword v153, v[68:69], off
	v_or_b32_e32 v68, 11, v2
	v_mad_u64_u32 v[68:69], s[12:13], v68, s14, v[100:101]
	v_lshl_add_u64 v[70:71], v[68:69], 0, s[16:17]
	global_load_dword v155, v[72:73], off
	v_lshl_add_u64 v[68:69], v[68:69], 0, s[18:19]
	v_lshl_add_u64 v[72:73], v[70:71], 0, v[84:85]
	v_lshl_add_u64 v[70:71], v[70:71], 0, v[86:87]
	global_load_dword v149, v[72:73], off
	global_load_dword v148, v[70:71], off
	v_lshl_add_u64 v[72:73], v[68:69], 0, v[84:85]
	v_lshl_add_u64 v[68:69], v[68:69], 0, v[86:87]
	global_load_dword v150, v[68:69], off
	v_or_b32_e32 v68, 16, v2
	v_mad_u64_u32 v[68:69], s[12:13], v68, s14, v[100:101]
	v_lshl_add_u64 v[70:71], v[68:69], 0, s[16:17]
	v_lshl_add_u64 v[68:69], v[68:69], 0, s[18:19]
	v_lshl_add_u64 v[88:89], v[70:71], 0, v[84:85]
	global_load_dword v151, v[72:73], off
	global_load_dword v146, v[88:89], off
	v_lshl_add_u64 v[88:89], v[68:69], 0, v[84:85]
	v_lshl_add_u64 v[70:71], v[70:71], 0, v[86:87]
	v_lshl_add_u64 v[68:69], v[68:69], 0, v[86:87]
	global_load_dword v143, v[70:71], off
	global_load_dword v144, v[68:69], off
	v_or_b32_e32 v68, 17, v2
	v_mad_u64_u32 v[68:69], s[12:13], v68, s14, v[100:101]
	v_lshl_add_u64 v[70:71], v[68:69], 0, s[16:17]
	global_load_dword v147, v[88:89], off
	v_lshl_add_u64 v[68:69], v[68:69], 0, s[18:19]
	v_lshl_add_u64 v[88:89], v[70:71], 0, v[84:85]
	v_lshl_add_u64 v[70:71], v[70:71], 0, v[86:87]
	global_load_dword v140, v[88:89], off
	global_load_dword v139, v[70:71], off
	v_lshl_add_u64 v[88:89], v[68:69], 0, v[84:85]
	v_lshl_add_u64 v[68:69], v[68:69], 0, v[86:87]
	global_load_dword v141, v[68:69], off
	v_or_b32_e32 v68, 18, v2
	v_mad_u64_u32 v[68:69], s[12:13], v68, s14, v[100:101]
	v_lshl_add_u64 v[70:71], v[68:69], 0, s[16:17]
	global_load_dword v142, v[88:89], off
	v_lshl_add_u64 v[68:69], v[68:69], 0, s[18:19]
	v_lshl_add_u64 v[88:89], v[70:71], 0, v[84:85]
	v_lshl_add_u64 v[70:71], v[70:71], 0, v[86:87]
	global_load_dword v137, v[88:89], off
	global_load_dword v135, v[70:71], off
	v_lshl_add_u64 v[88:89], v[68:69], 0, v[84:85]
	v_lshl_add_u64 v[68:69], v[68:69], 0, v[86:87]
	global_load_dword v136, v[68:69], off
	v_or_b32_e32 v68, 19, v2
	v_mad_u64_u32 v[68:69], s[12:13], v68, s14, v[100:101]
	v_lshl_add_u64 v[70:71], v[68:69], 0, s[16:17]
	global_load_dword v138, v[88:89], off
	v_lshl_add_u64 v[68:69], v[68:69], 0, s[18:19]
	v_lshl_add_u64 v[88:89], v[70:71], 0, v[84:85]
	v_lshl_add_u64 v[70:71], v[70:71], 0, v[86:87]
	global_load_dword v133, v[88:89], off
	global_load_dword v131, v[70:71], off
	v_lshl_add_u64 v[88:89], v[68:69], 0, v[84:85]
	v_lshlrev_b32_e32 v1, 2, v1
	global_load_dword v134, v[88:89], off
	v_lshl_add_u64 v[68:69], v[68:69], 0, v[86:87]
	v_or_b32_e32 v88, 24, v2
	global_load_dwordx4 v[80:83], v1, s[6:7]
	global_load_dwordx4 v[76:79], v1, s[6:7] offset:32
	global_load_dwordx4 v[72:75], v1, s[6:7] offset:64
	global_load_dword v132, v[68:69], off
	v_ashrrev_i32_e32 v185, 4, v176
	global_load_dwordx4 v[68:71], v1, s[6:7] offset:96
	v_mad_u64_u32 v[88:89], s[6:7], v88, s14, v[100:101]
	v_lshl_add_u64 v[90:91], v[88:89], 0, s[16:17]
	v_lshl_add_u64 v[88:89], v[88:89], 0, s[18:19]
	v_lshl_add_u64 v[92:93], v[90:91], 0, v[84:85]
	v_lshl_add_u64 v[90:91], v[90:91], 0, v[86:87]
	global_load_dword v129, v[92:93], off
	global_load_dword v127, v[90:91], off
	v_lshl_add_u64 v[92:93], v[88:89], 0, v[84:85]
	v_lshl_add_u64 v[88:89], v[88:89], 0, v[86:87]
	v_or_b32_e32 v1, 25, v2
	global_load_dword v128, v[88:89], off
	v_mad_u64_u32 v[88:89], s[6:7], v1, s14, v[100:101]
	v_lshl_add_u64 v[90:91], v[88:89], 0, s[16:17]
	global_load_dword v130, v[92:93], off
	v_lshl_add_u64 v[88:89], v[88:89], 0, s[18:19]
	v_lshl_add_u64 v[92:93], v[90:91], 0, v[84:85]
	v_lshl_add_u64 v[90:91], v[90:91], 0, v[86:87]
	global_load_dword v125, v[92:93], off
	global_load_dword v123, v[90:91], off
	v_lshl_add_u64 v[92:93], v[88:89], 0, v[84:85]
	v_lshl_add_u64 v[88:89], v[88:89], 0, v[86:87]
	v_or_b32_e32 v1, 26, v2
	global_load_dword v124, v[88:89], off
	v_mad_u64_u32 v[88:89], s[6:7], v1, s14, v[100:101]
	v_lshl_add_u64 v[90:91], v[88:89], 0, s[16:17]
	global_load_dword v126, v[92:93], off
	v_lshl_add_u64 v[88:89], v[88:89], 0, s[18:19]
	v_lshl_add_u64 v[92:93], v[90:91], 0, v[84:85]
	v_lshl_add_u64 v[90:91], v[90:91], 0, v[86:87]
	global_load_dword v121, v[92:93], off
	global_load_dword v119, v[90:91], off
	v_lshl_add_u64 v[92:93], v[88:89], 0, v[84:85]
	v_lshl_add_u64 v[88:89], v[88:89], 0, v[86:87]
	v_or_b32_e32 v1, 27, v2
	global_load_dword v120, v[88:89], off
	v_mad_u64_u32 v[88:89], s[6:7], v1, s14, v[100:101]
	v_lshl_add_u64 v[90:91], v[88:89], 0, s[16:17]
	v_lshl_add_u64 v[88:89], v[88:89], 0, s[18:19]
	global_load_dword v122, v[92:93], off
; __device__ __forceinline__ void unit(const bf16_t* proj, const float* stats  , const float* lng, const float* lnb, const float* sw, const float* sb, bf16_t* Y2, int un, LAS unsigned char* lds) {
;     ...
;     { const int sr = tid >> 4, sc = (tid & 15) * 8, ch = g * 128 + sc;
;       const f32x4 g0 = *(const f32x4*)(lng + ch), g1 = *(const f32x4*)(lng + ch + 4), b0 = *(const f32x4*)(lnb + ch), b1 = *(const f32x4*)(lnb + ch + 4);
;       float mus[4], rss[4];
;       { float2 pp[4];
; #pragma unroll
;         for (int q = 0; q < 4; ++q) pp[q] = *(const float2*)(stats + ((size_t)(R0 + sr + 32 * q) * 16 + (tid & 15)) * 2);
;         asm volatile("" ::: "memory");
; #pragma unroll
;         for (int q = 0; q < 4; ++q) { float s1 = pp[q].x, s2 = pp[q].y;
; #pragma unroll
;             for (int off = 1; off < 16; off <<= 1) { s1 += __shfl_xor(s1, off); s2 += __shfl_xor(s2, off); }
;             mus[q] = s1 * (1.0f / 1024.0f); rss[q] = __builtin_amdgcn_rsqf(fmaxf(s2 * (1.0f / 1024.0f) - mus[q] * mus[q], 0.f) + LN_EPS); } }
; #pragma unroll
;       for (int q = 0; q < 4; ++q) { const int s = sr + 32 * q, row = R0 + s; const u32x4 vv = *(const u32x4*)(proj + (size_t)row * NC + C_VC + ch);
	v_lshl_add_u64 v[92:93], v[90:91], 0, v[84:85]
	v_lshl_add_u64 v[84:85], v[88:89], 0, v[84:85]
	global_load_dword v109, v[92:93], off
	global_load_dword v115, v[84:85], off
	v_lshl_add_u64 v[84:85], v[90:91], 0, v[86:87]
	global_load_dword v1, v[84:85], off
	v_lshl_add_u64 v[84:85], v[88:89], 0, v[86:87]
	global_load_dword v107, v[84:85], off
	v_and_b32_e32 v84, 15, v176
	v_lshlrev_b32_e32 v102, 3, v84
	v_or_b32_e32 v191, s2, v102
	v_lshlrev_b32_e32 v96, 2, v191
	global_load_dwordx4 v[84:87], v96, s[0:1] offset:16
	global_load_dwordx4 v[92:95], v96, s[0:1]
	global_load_dwordx4 v[88:91], v96, s[4:5] offset:16
	s_nop 0
	global_load_dwordx4 v[96:99], v96, s[4:5]
	v_add_u32_e32 v110, s11, v185
	v_readlane_b32 s0, v254, 37
	v_mov_b32_e32 v103, v3
	v_readlane_b32 s1, v254, 38
	v_ashrrev_i32_e32 v111, 31, v110
	v_lshlrev_b64 v[104:105], 7, v[110:111]
	v_lshl_add_u64 v[102:103], s[0:1], 0, v[102:103]
	v_lshl_add_u64 v[112:113], v[102:103], 0, v[104:105]
	global_load_dwordx2 v[104:105], v[112:113], off
	s_movk_i32 s0, 0x2000
	v_add_co_u32_e32 v116, vcc, s0, v112
	s_movk_i32 s0, 0x3000
	s_nop 0
	v_addc_co_u32_e32 v117, vcc, 0, v113, vcc
	global_load_dwordx2 v[102:103], v[116:117], off offset:-4096
	global_load_dwordx2 v[186:187], v[116:117], off
	v_add_co_u32_e32 v112, vcc, s0, v112
	v_and_b32_e32 v106, 64, v229
	s_nop 0
	v_addc_co_u32_e32 v113, vcc, 0, v113, vcc
	v_add_u32_e32 v106, 64, v106
	v_xor_b32_e32 v108, 1, v229
	v_cmp_lt_i32_e32 vcc, v108, v106
	global_load_dwordx2 v[188:189], v[112:113], off
	s_mov_b32 s0, 0x3a800000
	v_cndmask_b32_e32 v108, v229, v108, vcc
	v_lshlrev_b32_e32 v145, 2, v108
	v_xor_b32_e32 v108, 2, v229
	v_cmp_lt_i32_e32 vcc, v108, v106
	s_movk_i32 s4, 0x4000
	v_and_b32_e32 v184, 63, v176
	v_cndmask_b32_e32 v108, v229, v108, vcc
	v_lshlrev_b32_e32 v111, 2, v108
	v_xor_b32_e32 v108, 4, v229
	v_cmp_lt_i32_e32 vcc, v108, v106
	s_cmpk_gt_u32 s10, 0xff
	s_waitcnt vmcnt(3)
	ds_bpermute_b32 v112, v145, v104
	ds_bpermute_b32 v113, v145, v105
	v_cndmask_b32_e32 v108, v229, v108, vcc
	v_lshlrev_b32_e32 v190, 2, v108
	v_xor_b32_e32 v108, 8, v229
	v_cmp_lt_i32_e32 vcc, v108, v106
	s_waitcnt lgkmcnt(0)
	v_pk_add_f32 v[104:105], v[104:105], v[112:113]
	ds_bpermute_b32 v112, v111, v104
	ds_bpermute_b32 v113, v111, v105
	v_cndmask_b32_e32 v106, v229, v108, vcc
	v_lshlrev_b32_e32 v106, 2, v106
	s_waitcnt lgkmcnt(0)
	v_pk_add_f32 v[104:105], v[104:105], v[112:113]
	ds_bpermute_b32 v112, v190, v104
	ds_bpermute_b32 v113, v190, v105
	s_waitcnt lgkmcnt(0)
	v_pk_add_f32 v[104:105], v[104:105], v[112:113]
	ds_bpermute_b32 v112, v106, v104
	ds_bpermute_b32 v113, v106, v105
	s_waitcnt lgkmcnt(0)
	v_pk_add_f32 v[104:105], v[104:105], v[112:113]
	s_nop 0
	v_pk_mul_f32 v[116:117], v[104:105], s[0:1] op_sel_hi:[1,0]
	s_waitcnt vmcnt(2)
	ds_bpermute_b32 v105, v145, v103
	v_fma_f32 v104, -v116, v116, v117
	v_max_f32_e32 v104, 0, v104
	v_add_f32_e32 v104, 0x3727c5ac, v104
	v_rsq_f32_e32 v118, v104
	ds_bpermute_b32 v104, v145, v102
	s_waitcnt lgkmcnt(0)
	v_pk_add_f32 v[102:103], v[102:103], v[104:105]
	ds_bpermute_b32 v104, v111, v102
	ds_bpermute_b32 v105, v111, v103
	s_waitcnt lgkmcnt(0)
	v_pk_add_f32 v[102:103], v[102:103], v[104:105]
	ds_bpermute_b32 v104, v190, v102
	ds_bpermute_b32 v105, v190, v103
	s_waitcnt lgkmcnt(0)
	v_pk_add_f32 v[102:103], v[102:103], v[104:105]
	ds_bpermute_b32 v104, v106, v102
	ds_bpermute_b32 v105, v106, v103
	s_waitcnt lgkmcnt(0)
	v_pk_add_f32 v[102:103], v[102:103], v[104:105]
	s_nop 0
	v_pk_mul_f32 v[112:113], v[102:103], s[0:1] op_sel_hi:[1,0]
	s_waitcnt vmcnt(1)
	ds_bpermute_b32 v103, v145, v187
	v_fma_f32 v102, -v112, v112, v113
	v_max_f32_e32 v102, 0, v102
	v_add_f32_e32 v102, 0x3727c5ac, v102
	v_rsq_f32_e32 v114, v102
	ds_bpermute_b32 v102, v145, v186
	s_waitcnt lgkmcnt(0)
	v_pk_add_f32 v[102:103], v[186:187], v[102:103]
	ds_bpermute_b32 v104, v111, v102
	ds_bpermute_b32 v105, v111, v103
	s_waitcnt lgkmcnt(0)
	v_pk_add_f32 v[102:103], v[102:103], v[104:105]
	ds_bpermute_b32 v104, v190, v102
	ds_bpermute_b32 v105, v190, v103
	s_waitcnt lgkmcnt(0)
	v_pk_add_f32 v[102:103], v[102:103], v[104:105]
	ds_bpermute_b32 v104, v106, v102
	ds_bpermute_b32 v105, v106, v103
	s_waitcnt lgkmcnt(0)
	v_pk_add_f32 v[102:103], v[102:103], v[104:105]
	s_nop 0
	v_pk_mul_f32 v[102:103], v[102:103], s[0:1] op_sel_hi:[1,0]
	s_waitcnt vmcnt(0)
	ds_bpermute_b32 v105, v145, v189
	v_fma_f32 v104, -v102, v102, v103
	v_max_f32_e32 v104, 0, v104
	v_add_f32_e32 v104, 0x3727c5ac, v104
	v_rsq_f32_e32 v108, v104
	ds_bpermute_b32 v104, v145, v188
	s_waitcnt lgkmcnt(0)
	v_pk_add_f32 v[104:105], v[188:189], v[104:105]
	ds_bpermute_b32 v186, v111, v104
	ds_bpermute_b32 v187, v111, v105
	v_lshlrev_b32_e32 v111, 1, v185
	v_bfe_u32 v188, v176, 2, 2
	s_waitcnt lgkmcnt(0)
	v_pk_add_f32 v[104:105], v[104:105], v[186:187]
	ds_bpermute_b32 v186, v190, v104
	ds_bpermute_b32 v187, v190, v105
	s_waitcnt lgkmcnt(0)
	v_pk_add_f32 v[104:105], v[104:105], v[186:187]
	ds_bpermute_b32 v186, v106, v104
	ds_bpermute_b32 v187, v106, v105
	s_waitcnt lgkmcnt(0)
	v_pk_add_f32 v[104:105], v[104:105], v[186:187]
	v_and_b32_e32 v187, 8, v111
	v_lshrrev_b32_e32 v111, 1, v185
	v_and_b32_e32 v186, 3, v185
	v_and_or_b32 v111, v111, 4, v186
	v_pk_mul_f32 v[104:105], v[104:105], s[0:1] op_sel_hi:[1,0]
	v_lshlrev_b32_e32 v189, 6, v111
	v_mad_i64_i32 v[192:193], s[0:1], v110, s14, v[100:101]
	v_lshlrev_b32_e32 v110, 1, v191
	v_mov_b32_e32 v111, v3
	v_lshl_add_u64 v[192:193], v[192:193], 0, v[110:111]
	v_add_co_u32_e32 v192, vcc, s4, v192
	v_lshlrev_b32_e32 v186, 4, v176
	s_nop 0
	v_addc_co_u32_e32 v193, vcc, 0, v193, vcc
	global_load_dwordx4 v[196:199], v[192:193], off offset:2048
	s_mov_b64 s[100:101], 0x1d0000
	v_lshl_add_u64 v[248:249], v[192:193], 0, s[100:101]
	global_load_dwordx4 v[248:251], v[248:249], off offset:2048
	v_and_b32_e32 v190, 48, v186
	v_fma_f32 v106, -v104, v104, v105
	v_max_f32_e32 v106, 0, v106
	v_add_f32_e32 v106, 0x3727c5ac, v106
	v_rsq_f32_e32 v106, v106
	s_waitcnt vmcnt(1)
; __device__ __forceinline__ unsigned cvt_pk_bf16(float lo, float hi) { f32x2_t v = {lo, hi}; bf16x2_t b = __builtin_convertvector(v, bf16x2_t); return __builtin_bit_cast(unsigned, b); }
; #define LAS __attribute__((address_space(3)))
; __device__ __forceinline__ float bflo(unsigned w) { return __uint_as_float(w << 16); }
; __device__ __forceinline__ float bfhi(unsigned w) { return __uint_as_float(w & 0xffff0000u); }
; __device__ __forceinline__ int v_st(int k, int c) { const int kk = (k & ~0xC) | ((k & 4) << 1) | ((k & 8) >> 1); return ((kk >> 3) * 4 + (c >> 5)) * 512 + ((kk & 7) * 32 + (c & 31)) * 2; }
; __device__ __forceinline__ void unit(const bf16_t* proj, const float* stats  , const float* lng, const float* lnb, const float* sw, const float* sb, bf16_t* Y2, int un, LAS unsigned char* lds) {
;     ...
;         for (int q = 0; q < 4; ++q) { float s1 = pp[q].x, s2 = pp[q].y;
; #pragma unroll
;             for (int off = 1; off < 16; off <<= 1) { s1 += __shfl_xor(s1, off); s2 += __shfl_xor(s2, off); }
;             mus[q] = s1 * (1.0f / 1024.0f); rss[q] = __builtin_amdgcn_rsqf(fmaxf(s2 * (1.0f / 1024.0f) - mus[q] * mus[q], 0.f) + LN_EPS); } }
; #pragma unroll
;       for (int q = 0; q < 4; ++q) { const int s = sr + 32 * q, row = R0 + s; const u32x4 vv = *(const u32x4*)(proj + (size_t)row * NC + C_VC + ch);
;           const float mu = mus[q], rs = rss[q];
;           u32x4 w; w.x = pg8::cvt_pk_bf16((bflo(vv.x) - mu) * rs * g0[0] + b0[0], (bfhi(vv.x) - mu) * rs * g0[1] + b0[1]); w.y = pg8::cvt_pk_bf16((bflo(vv.y) - mu) * rs * g0[2] + b0[2], (bfhi(vv.y) - mu) * rs * g0[3] + b0[3]);
;           w.z = pg8::cvt_pk_bf16((bflo(vv.z) - mu) * rs * g1[0] + b1[0], (bfhi(vv.z) - mu) * rs * g1[1] + b1[1]); w.w = pg8::cvt_pk_bf16((bflo(vv.w) - mu) * rs * g1[2] + b1[2], (bfhi(vv.w) - mu) * rs * g1[3] + b1[3]);
;           *(LAS u32x4*)(lds + (s >> 6) * att::SHM_V + att::v_st(s & 63, sc)) = w; } }
	v_lshlrev_b32_e32 v192, 16, v196
	v_and_b32_e32 v193, 0xffff0000, v196
	v_pk_add_f32 v[192:193], v[192:193], v[116:117] op_sel_hi:[1,0] neg_lo:[0,1] neg_hi:[0,1]
	s_nop 0
	v_pk_mul_f32 v[192:193], v[118:119], v[192:193] op_sel_hi:[0,1]
	v_pk_fma_f32 v[192:193], v[92:93], v[192:193], v[96:97]
	s_nop 0
	v_cvt_pk_bf16_f32 v196, v192, v193
	v_lshlrev_b32_e32 v192, 16, v197
	v_and_b32_e32 v193, 0xffff0000, v197
	v_pk_add_f32 v[192:193], v[192:193], v[116:117] op_sel_hi:[1,0] neg_lo:[0,1] neg_hi:[0,1]
	s_nop 0
	v_pk_mul_f32 v[192:193], v[118:119], v[192:193] op_sel_hi:[0,1]
	v_pk_fma_f32 v[192:193], v[94:95], v[192:193], v[98:99]
	s_nop 0
	v_cvt_pk_bf16_f32 v197, v192, v193
	v_lshlrev_b32_e32 v192, 16, v198
	v_and_b32_e32 v193, 0xffff0000, v198
	v_pk_add_f32 v[192:193], v[192:193], v[116:117] op_sel_hi:[1,0] neg_lo:[0,1] neg_hi:[0,1]
	s_nop 0
	v_pk_mul_f32 v[192:193], v[118:119], v[192:193] op_sel_hi:[0,1]
	v_pk_fma_f32 v[192:193], v[84:85], v[192:193], v[88:89]
	s_nop 0
	v_cvt_pk_bf16_f32 v198, v192, v193
	v_lshlrev_b32_e32 v192, 16, v199
	v_and_b32_e32 v193, 0xffff0000, v199
	v_pk_add_f32 v[116:117], v[192:193], v[116:117] op_sel_hi:[1,0] neg_lo:[0,1] neg_hi:[0,1]
	s_nop 0
	v_pk_mul_f32 v[116:117], v[118:119], v[116:117] op_sel_hi:[0,1]
	v_pk_fma_f32 v[116:117], v[86:87], v[116:117], v[90:91]
	s_nop 0
	v_cvt_pk_bf16_f32 v199, v116, v117
	v_lshlrev_b32_e32 v116, 8, v185
	v_and_b32_e32 v117, 0xffffc000, v116
	v_and_or_b32 v116, v185, 48, v187
	v_lshrrev_b32_e32 v116, 1, v116
	v_or_b32_e32 v116, v116, v188
	v_lshlrev_b32_e32 v116, 9, v116
	v_add3_u32 v117, 0, v117, v116
	v_add3_u32 v117, v117, v189, v190
	ds_write_b128 v117, v[196:199]
	v_add_u32_e32 v117, 32, v185
	v_add_u32_e32 v118, s11, v117
	v_mad_i64_i32 v[192:193], s[0:1], v118, s14, v[100:101]
	v_lshl_add_u64 v[192:193], v[192:193], 0, v[110:111]
	v_add_co_u32_e32 v192, vcc, s4, v192
	s_nop 1
	v_addc_co_u32_e32 v193, vcc, 0, v193, vcc
	s_waitcnt vmcnt(0)
	v_lshlrev_b32_e32 v192, 16, v248
	v_and_b32_e32 v193, 0xffff0000, v248
	v_pk_add_f32 v[192:193], v[192:193], v[112:113] op_sel_hi:[1,0] neg_lo:[0,1] neg_hi:[0,1]
	s_nop 0
	v_pk_mul_f32 v[192:193], v[114:115], v[192:193] op_sel_hi:[0,1]
	v_pk_fma_f32 v[192:193], v[92:93], v[192:193], v[96:97]
	s_nop 0
	v_cvt_pk_bf16_f32 v248, v192, v193
	v_lshlrev_b32_e32 v192, 16, v249
	v_and_b32_e32 v193, 0xffff0000, v249
	v_pk_add_f32 v[192:193], v[192:193], v[112:113] op_sel_hi:[1,0] neg_lo:[0,1] neg_hi:[0,1]
	s_nop 0
	v_pk_mul_f32 v[192:193], v[114:115], v[192:193] op_sel_hi:[0,1]
	v_pk_fma_f32 v[192:193], v[94:95], v[192:193], v[98:99]
	s_nop 0
	v_cvt_pk_bf16_f32 v249, v192, v193
	v_lshlrev_b32_e32 v192, 16, v250
	v_and_b32_e32 v193, 0xffff0000, v250
	v_pk_add_f32 v[192:193], v[192:193], v[112:113] op_sel_hi:[1,0] neg_lo:[0,1] neg_hi:[0,1]
	s_nop 0
	v_pk_mul_f32 v[192:193], v[114:115], v[192:193] op_sel_hi:[0,1]
	v_pk_fma_f32 v[192:193], v[84:85], v[192:193], v[88:89]
	s_nop 0
	v_cvt_pk_bf16_f32 v250, v192, v193
	v_lshlrev_b32_e32 v192, 16, v251
	v_and_b32_e32 v193, 0xffff0000, v251
	v_pk_add_f32 v[112:113], v[192:193], v[112:113] op_sel_hi:[1,0] neg_lo:[0,1] neg_hi:[0,1]
	s_nop 0
	v_pk_mul_f32 v[112:113], v[114:115], v[112:113] op_sel_hi:[0,1]
	v_pk_fma_f32 v[112:113], v[86:87], v[112:113], v[90:91]
	v_add_u32_e32 v114, 64, v185
	v_cvt_pk_bf16_f32 v251, v112, v113
	v_and_or_b32 v113, v117, 48, v187
	v_lshrrev_b32_e32 v113, 1, v113
	v_lshlrev_b32_e32 v112, 8, v117
	v_or_b32_e32 v113, v113, v188
	v_and_b32_e32 v112, 0xffffc000, v112
	v_lshlrev_b32_e32 v113, 9, v113
	v_add3_u32 v112, 0, v112, v113
	v_add3_u32 v112, v112, v189, v190
	ds_write_b128 v112, v[248:251]
	v_add_u32_e32 v112, s11, v114
	v_mad_i64_i32 v[112:113], s[0:1], v112, s14, v[100:101]
	v_lshl_add_u64 v[112:113], v[112:113], 0, v[110:111]
	v_add_co_u32_e32 v112, vcc, s4, v112
	s_nop 1
	v_addc_co_u32_e32 v113, vcc, 0, v113, vcc
	global_load_dwordx4 v[196:199], v[112:113], off offset:2048
	s_mov_b64 s[100:101], 0x1d0000
	v_lshl_add_u64 v[248:249], v[112:113], 0, s[100:101]
	global_load_dwordx4 v[248:251], v[248:249], off offset:2048
	s_waitcnt vmcnt(1)
	v_lshlrev_b32_e32 v112, 16, v196
	v_and_b32_e32 v113, 0xffff0000, v196
	v_pk_add_f32 v[112:113], v[112:113], v[102:103] op_sel_hi:[1,0] neg_lo:[0,1] neg_hi:[0,1]
	s_nop 0
	v_pk_mul_f32 v[112:113], v[108:109], v[112:113] op_sel_hi:[0,1]
	v_pk_fma_f32 v[112:113], v[92:93], v[112:113], v[96:97]
	s_nop 0
	v_cvt_pk_bf16_f32 v196, v112, v113
	v_lshlrev_b32_e32 v112, 16, v197
	v_and_b32_e32 v113, 0xffff0000, v197
	v_pk_add_f32 v[112:113], v[112:113], v[102:103] op_sel_hi:[1,0] neg_lo:[0,1] neg_hi:[0,1]
	s_nop 0
	v_pk_mul_f32 v[112:113], v[108:109], v[112:113] op_sel_hi:[0,1]
	v_pk_fma_f32 v[112:113], v[94:95], v[112:113], v[98:99]
	s_nop 0
	v_cvt_pk_bf16_f32 v197, v112, v113
	v_lshlrev_b32_e32 v112, 16, v198
	v_and_b32_e32 v113, 0xffff0000, v198
	v_pk_add_f32 v[112:113], v[112:113], v[102:103] op_sel_hi:[1,0] neg_lo:[0,1] neg_hi:[0,1]
	s_nop 0
	v_pk_mul_f32 v[112:113], v[108:109], v[112:113] op_sel_hi:[0,1]
	v_pk_fma_f32 v[112:113], v[84:85], v[112:113], v[88:89]
	s_nop 0
	v_cvt_pk_bf16_f32 v198, v112, v113
	v_lshlrev_b32_e32 v112, 16, v199
	v_and_b32_e32 v113, 0xffff0000, v199
	v_pk_add_f32 v[102:103], v[112:113], v[102:103] op_sel_hi:[1,0] neg_lo:[0,1] neg_hi:[0,1]
	s_nop 0
	v_pk_mul_f32 v[102:103], v[108:109], v[102:103] op_sel_hi:[0,1]
	v_pk_fma_f32 v[102:103], v[86:87], v[102:103], v[90:91]
	v_add_u32_e32 v108, 0x60, v185
	v_cvt_pk_bf16_f32 v199, v102, v103
	v_lshlrev_b32_e32 v102, 8, v114
	v_and_b32_e32 v102, 0xffffc000, v102
	v_add3_u32 v102, 0, v102, v116
	v_add3_u32 v102, v102, v189, v190
	ds_write_b128 v102, v[196:199]
	v_add_u32_e32 v102, s11, v108
	v_mad_i64_i32 v[100:101], s[0:1], v102, s14, v[100:101]
	v_lshl_add_u64 v[100:101], v[100:101], 0, v[110:111]
	v_add_co_u32_e32 v100, vcc, s4, v100
	s_cselect_b64 s[0:1], -1, 0
	s_nop 0
	v_addc_co_u32_e32 v101, vcc, 0, v101, vcc
	v_cmp_le_u32_e32 vcc, v183, v182
	s_mov_b64 s[4:5], -1
	s_waitcnt vmcnt(0)
; __device__ __forceinline__ unsigned cvt_pk_bf16(float lo, float hi) { f32x2_t v = {lo, hi}; bf16x2_t b = __builtin_convertvector(v, bf16x2_t); return __builtin_bit_cast(unsigned, b); }
; #define LAS __attribute__((address_space(3)))
; __device__ __forceinline__ float bflo(unsigned w) { return __uint_as_float(w << 16); }
; __device__ __forceinline__ float bfhi(unsigned w) { return __uint_as_float(w & 0xffff0000u); }
; __device__ __forceinline__ void unit(const bf16_t* proj, const float* stats  , const float* lng, const float* lnb, const float* sw, const float* sb, bf16_t* Y2, int un, LAS unsigned char* lds) {
;     ...
;       for (int q = 0; q < 4; ++q) { const int s = sr + 32 * q, row = R0 + s; const u32x4 vv = *(const u32x4*)(proj + (size_t)row * NC + C_VC + ch);
;           const float mu = mus[q], rs = rss[q];
;           u32x4 w; w.x = pg8::cvt_pk_bf16((bflo(vv.x) - mu) * rs * g0[0] + b0[0], (bfhi(vv.x) - mu) * rs * g0[1] + b0[1]); w.y = pg8::cvt_pk_bf16((bflo(vv.y) - mu) * rs * g0[2] + b0[2], (bfhi(vv.y) - mu) * rs * g0[3] + b0[3]);
;           w.z = pg8::cvt_pk_bf16((bflo(vv.z) - mu) * rs * g1[0] + b1[0], (bfhi(vv.z) - mu) * rs * g1[1] + b1[1]); w.w = pg8::cvt_pk_bf16((bflo(vv.w) - mu) * rs * g1[2] + b1[2], (bfhi(vv.w) - mu) * rs * g1[3] + b1[3]);
;           *(LAS u32x4*)(lds + (s >> 6) * att::SHM_V + att::v_st(s & 63, sc)) = w; } }
;     ...
;         if (st * 64 > tb * 32 + 31) continue;
;         att::bf16x8 pa[4];
; #pragma unroll
;         for (int k = 0; k < 4; ++k) { const int s0 = st * 64 + 16 * k + hi * 8; const f32x4 w0 = wv[2 * (st * 4 + k)], w1 = wv[2 * (st * 4 + k) + 1];
;             float x[8] = {w0[0], w0[1], w0[2], w0[3], w1[0], w1[1], w1[2], w1[3]};
; #pragma unroll
;             for (int j = 0; j < 8; ++j) x[j] = (s0 + j <= t) ? x[j] : 0.f;
;             u32x4 p; p.x = pg8::cvt_pk_bf16(x[0], x[1]); p.y = pg8::cvt_pk_bf16(x[2], x[3]); p.z = pg8::cvt_pk_bf16(x[4], x[5]); p.w = pg8::cvt_pk_bf16(x[6], x[7]); pa[k] = __builtin_bit_cast(att::bf16x8, p); }
;         if (eh == 0) { att::pv_one<0>(o0, vb + st * att::SHM_V, pa[0], pa[1], pa[2], pa[3]); att::pv_one<1>(o1, vb + st * att::SHM_V, pa[0], pa[1], pa[2], pa[3]); }
;         else         { att::pv_one<2>(o0, vb + st * att::SHM_V, pa[0], pa[1], pa[2], pa[3]); att::pv_one<3>(o1, vb + st * att::SHM_V, pa[0], pa[1], pa[2], pa[3]); }
	v_lshlrev_b32_e32 v110, 16, v248
	v_and_b32_e32 v111, 0xffff0000, v248
	v_pk_add_f32 v[110:111], v[110:111], v[104:105] op_sel_hi:[1,0] neg_lo:[0,1] neg_hi:[0,1]
	v_cndmask_b32_e32 v32, 0, v32, vcc
	v_pk_mul_f32 v[110:111], v[106:107], v[110:111] op_sel_hi:[0,1]
	v_pk_fma_f32 v[92:93], v[92:93], v[110:111], v[96:97]
	v_lshlrev_b32_e32 v96, 16, v249
	v_and_b32_e32 v97, 0xffff0000, v249
	v_pk_add_f32 v[96:97], v[96:97], v[104:105] op_sel_hi:[1,0] neg_lo:[0,1] neg_hi:[0,1]
	v_cvt_pk_bf16_f32 v92, v92, v93
	v_pk_mul_f32 v[96:97], v[106:107], v[96:97] op_sel_hi:[0,1]
	v_pk_fma_f32 v[94:95], v[94:95], v[96:97], v[98:99]
	v_cmp_lt_u32_e32 vcc, v183, v182
	v_cvt_pk_bf16_f32 v93, v94, v95
	v_lshlrev_b32_e32 v94, 16, v250
	v_and_b32_e32 v95, 0xffff0000, v250
	v_pk_add_f32 v[94:95], v[94:95], v[104:105] op_sel_hi:[1,0] neg_lo:[0,1] neg_hi:[0,1]
	v_cndmask_b32_e32 v33, 0, v33, vcc
	v_pk_mul_f32 v[94:95], v[106:107], v[94:95] op_sel_hi:[0,1]
	v_pk_fma_f32 v[84:85], v[84:85], v[94:95], v[88:89]
	s_nop 0
	v_cvt_pk_bf16_f32 v94, v84, v85
	v_lshlrev_b32_e32 v84, 16, v251
	v_and_b32_e32 v85, 0xffff0000, v251
	v_pk_add_f32 v[84:85], v[84:85], v[104:105] op_sel_hi:[1,0] neg_lo:[0,1] neg_hi:[0,1]
	s_nop 0
	v_pk_mul_f32 v[84:85], v[106:107], v[84:85] op_sel_hi:[0,1]
	v_pk_fma_f32 v[84:85], v[86:87], v[84:85], v[90:91]
	v_and_b32_e32 v86, 0xc0, v186
	v_cvt_pk_bf16_f32 v95, v84, v85
	v_and_or_b32 v85, v108, 48, v187
	v_lshrrev_b32_e32 v85, 1, v85
	v_lshlrev_b32_e32 v84, 8, v108
	v_or_b32_e32 v85, v85, v188
	v_and_b32_e32 v84, 0xffffc000, v84
	v_lshlrev_b32_e32 v85, 9, v85
	v_add3_u32 v84, 0, v84, v85
	v_add3_u32 v84, v84, v189, v190
	ds_write_b128 v84, v[92:95]
	v_lshlrev_b32_e32 v84, 3, v184
	v_and_b32_e32 v85, 24, v84
	v_lshlrev_b32_e32 v87, 1, v176
	v_and_b32_e32 v87, 32, v87
	v_and_b32_e32 v84, 0x100, v84
	v_add3_u32 v85, 0, v85, v86
	v_add3_u32 v100, v85, v87, v84
	v_or_b32_e32 v84, 2, v183
	v_cmp_le_u32_e32 vcc, v84, v182
	v_or_b32_e32 v84, 3, v183
	s_waitcnt lgkmcnt(0)
	v_cndmask_b32_e32 v34, 0, v34, vcc
	v_cmp_le_u32_e32 vcc, v84, v182
	v_or_b32_e32 v84, 4, v183
	s_barrier
	v_cndmask_b32_e32 v35, 0, v35, vcc
	v_cmp_le_u32_e32 vcc, v84, v182
	v_or_b32_e32 v84, 5, v183
	v_cvt_pk_bf16_f32 v85, v34, v35
	v_cndmask_b32_e32 v28, 0, v28, vcc
	v_cmp_le_u32_e32 vcc, v84, v182
	v_or_b32_e32 v84, 6, v183
	s_nop 0
	v_cndmask_b32_e32 v29, 0, v29, vcc
	v_cmp_le_u32_e32 vcc, v84, v182
	v_or_b32_e32 v84, 7, v183
	v_cvt_pk_bf16_f32 v86, v28, v29
	v_cndmask_b32_e32 v30, 0, v30, vcc
	v_cmp_le_u32_e32 vcc, v84, v182
	v_or_b32_e32 v28, 16, v183
	v_cvt_pk_bf16_f32 v84, v32, v33
	v_cndmask_b32_e32 v31, 0, v31, vcc
	v_cmp_le_u32_e32 vcc, v28, v182
	v_or_b32_e32 v28, 17, v183
	v_cvt_pk_bf16_f32 v87, v30, v31
	v_cndmask_b32_e32 v24, 0, v24, vcc
	v_cmp_le_u32_e32 vcc, v28, v182
	v_or_b32_e32 v28, 18, v183
	s_nop 0
	v_cndmask_b32_e32 v25, 0, v25, vcc
	v_cmp_le_u32_e32 vcc, v28, v182
	v_or_b32_e32 v28, 19, v183
	v_cvt_pk_bf16_f32 v88, v24, v25
	v_cndmask_b32_e32 v26, 0, v26, vcc
	v_cmp_le_u32_e32 vcc, v28, v182
	v_or_b32_e32 v28, 20, v183
	s_nop 0
	v_cndmask_b32_e32 v27, 0, v27, vcc
	v_cmp_le_u32_e32 vcc, v28, v182
	v_or_b32_e32 v28, 21, v183
	v_cvt_pk_bf16_f32 v89, v26, v27
	v_cndmask_b32_e32 v20, 0, v20, vcc
	v_cmp_le_u32_e32 vcc, v28, v182
	v_or_b32_e32 v28, 22, v183
	s_nop 0
	v_cndmask_b32_e32 v21, 0, v21, vcc
	v_cmp_le_u32_e32 vcc, v28, v182
	v_or_b32_e32 v28, 23, v183
	v_cvt_pk_bf16_f32 v90, v20, v21
	v_cndmask_b32_e32 v22, 0, v22, vcc
	v_cmp_le_u32_e32 vcc, v28, v182
	v_or_b32_e32 v20, 32, v183
	s_nop 0
	v_cndmask_b32_e32 v23, 0, v23, vcc
	v_cmp_le_u32_e32 vcc, v20, v182
	v_or_b32_e32 v20, 33, v183
	v_cvt_pk_bf16_f32 v91, v22, v23
	v_cndmask_b32_e32 v16, 0, v16, vcc
	v_cmp_le_u32_e32 vcc, v20, v182
	v_or_b32_e32 v20, 34, v183
	s_nop 0
	v_cndmask_b32_e32 v17, 0, v17, vcc
	v_cmp_le_u32_e32 vcc, v20, v182
	v_or_b32_e32 v20, 35, v183
	v_cvt_pk_bf16_f32 v96, v16, v17
	v_cndmask_b32_e32 v18, 0, v18, vcc
	v_cmp_le_u32_e32 vcc, v20, v182
	v_or_b32_e32 v20, 36, v183
	s_nop 0
	v_cndmask_b32_e32 v19, 0, v19, vcc
	v_cmp_le_u32_e32 vcc, v20, v182
	v_or_b32_e32 v20, 37, v183
	v_cvt_pk_bf16_f32 v97, v18, v19
	v_cndmask_b32_e32 v12, 0, v12, vcc
	v_cmp_le_u32_e32 vcc, v20, v182
	v_or_b32_e32 v20, 38, v183
	s_nop 0
	v_cndmask_b32_e32 v13, 0, v13, vcc
	v_cmp_le_u32_e32 vcc, v20, v182
	v_or_b32_e32 v20, 39, v183
	v_cvt_pk_bf16_f32 v98, v12, v13
	v_cndmask_b32_e32 v14, 0, v14, vcc
	v_cmp_le_u32_e32 vcc, v20, v182
	v_or_b32_e32 v12, 48, v183
	s_nop 0
	v_cndmask_b32_e32 v15, 0, v15, vcc
	v_cmp_le_u32_e32 vcc, v12, v182
	v_or_b32_e32 v12, 49, v183
	v_cvt_pk_bf16_f32 v99, v14, v15
	v_cndmask_b32_e32 v8, 0, v8, vcc
	v_cmp_le_u32_e32 vcc, v12, v182
	v_or_b32_e32 v12, 50, v183
	s_nop 0
	v_cndmask_b32_e32 v9, 0, v9, vcc
	v_cmp_le_u32_e32 vcc, v12, v182
	v_or_b32_e32 v12, 51, v183
	v_cvt_pk_bf16_f32 v92, v8, v9
	v_cndmask_b32_e32 v10, 0, v10, vcc
	v_cmp_le_u32_e32 vcc, v12, v182
	v_or_b32_e32 v12, 52, v183
	s_nop 0
	v_cndmask_b32_e32 v11, 0, v11, vcc
	v_cmp_le_u32_e32 vcc, v12, v182
	v_or_b32_e32 v12, 53, v183
	v_cvt_pk_bf16_f32 v93, v10, v11
	v_cndmask_b32_e32 v4, 0, v4, vcc
	v_cmp_le_u32_e32 vcc, v12, v182
	v_or_b32_e32 v12, 54, v183
	s_nop 0
	v_cndmask_b32_e32 v5, 0, v5, vcc
	v_cmp_le_u32_e32 vcc, v12, v182
	v_or_b32_e32 v12, 55, v183
	v_cvt_pk_bf16_f32 v94, v4, v5
	v_cndmask_b32_e32 v6, 0, v6, vcc
	v_cmp_le_u32_e32 vcc, v12, v182
	s_nop 1
	v_cndmask_b32_e32 v7, 0, v7, vcc
	v_cvt_pk_bf16_f32 v95, v6, v7
	s_and_b64 vcc, exec, s[0:1]
	s_cbranch_vccz .LBB0_1379
	ds_read_b64_tr_b16 v[4:5], v100 offset:1024
	ds_read_b64_tr_b16 v[6:7], v100 offset:3072
	ds_read_b64_tr_b16 v[20:21], v100 offset:5120
	ds_read_b64_tr_b16 v[22:23], v100 offset:7168
	s_mov_b64 s[4:5], 0
	s_waitcnt lgkmcnt(2)
	v_mfma_f32_32x32x16_bf16 v[4:19], v[84:87], v[4:7], 0
	s_waitcnt lgkmcnt(0)
	v_mfma_f32_32x32x16_bf16 v[4:19], v[88:91], v[20:23], v[4:19]
	ds_read_b64_tr_b16 v[20:21], v100 offset:9216
	ds_read_b64_tr_b16 v[22:23], v100 offset:11264
	s_waitcnt lgkmcnt(0)
	v_mfma_f32_32x32x16_bf16 v[4:19], v[96:99], v[20:23], v[4:19]
	ds_read_b64_tr_b16 v[20:21], v100 offset:13312
	ds_read_b64_tr_b16 v[22:23], v100 offset:15360
	s_waitcnt lgkmcnt(0)
	v_mfma_f32_32x32x16_bf16 v[4:19], v[92:95], v[20:23], v[4:19]
	ds_read_b64_tr_b16 v[22:23], v100 offset:3584
	ds_read_b64_tr_b16 v[20:21], v100 offset:1536
	ds_read_b64_tr_b16 v[104:105], v100 offset:7680
	ds_read_b64_tr_b16 v[102:103], v100 offset:5632
	s_waitcnt lgkmcnt(2)
	v_mfma_f32_32x32x16_bf16 v[20:35], v[84:87], v[20:23], 0
	s_waitcnt lgkmcnt(0)
	v_mfma_f32_32x32x16_bf16 v[20:35], v[88:91], v[102:105], v[20:35]
	ds_read_b64_tr_b16 v[104:105], v100 offset:11776
	ds_read_b64_tr_b16 v[102:103], v100 offset:9728
	s_waitcnt lgkmcnt(0)
	v_mfma_f32_32x32x16_bf16 v[20:35], v[96:99], v[102:105], v[20:35]
	ds_read_b64_tr_b16 v[104:105], v100 offset:15872
	ds_read_b64_tr_b16 v[102:103], v100 offset:13824
	s_waitcnt lgkmcnt(0)
	v_mfma_f32_32x32x16_bf16 v[20:35], v[92:95], v[102:105], v[20:35]
